# as previous, plus expert 5 converted during the sequential recurrence phase instead of the prologue (prologue: experts 0-1, beside first GEMM: 2-4, recurrence phase: 5-7)
# speedup vs baseline: 1.0166x; 1.0005x over previous
_Z10hybrid_fwd4Args:
	s_load_dwordx8 s[52:59], s[0:1], 0x100
	s_load_dwordx2 s[76:77], s[0:1], 0x120
	s_mov_b32 s96, s2
	v_cmp_gt_u32_e64 s[4:5], 64, v0
	s_and_saveexec_b64 s[2:3], s[4:5]
	v_lshl_add_u32 v1, v0, 2, 0
	v_add_u32_e32 v1, 0x26000, v1
	v_mov_b32_e32 v2, 0
	ds_write_b32 v1, v2
	s_or_b64 exec, exec, s[2:3]
	s_load_dwordx16 s[8:23], s[0:1], 0x40
	s_load_dwordx16 s[80:95], s[0:1], 0xc0
	s_waitcnt lgkmcnt(0)
	s_mov_b32 s98, 0
	s_mov_b32 s99, 0
	s_mov_b32 s100, 2
	s_barrier
	v_writelane_b32 v239, s8, 0
	s_getreg_b32 s2, hwreg(HW_REG_XCC_ID, 0, 4)
	s_and_b32 s78, s2, 15
	v_writelane_b32 v239, s9, 1
	v_writelane_b32 v239, s10, 2
	v_writelane_b32 v239, s11, 3
	v_writelane_b32 v239, s12, 4
	v_writelane_b32 v239, s13, 5
	v_writelane_b32 v239, s14, 6
	v_writelane_b32 v239, s15, 7
	v_writelane_b32 v239, s16, 8
	v_writelane_b32 v239, s17, 9
	v_writelane_b32 v239, s18, 10
	v_writelane_b32 v239, s19, 11
	v_writelane_b32 v239, s20, 12
	v_writelane_b32 v239, s21, 13
	v_writelane_b32 v239, s22, 14
	v_writelane_b32 v239, s23, 15
	v_cmp_eq_u32_e64 s[6:7], 0, v0
	s_mov_b64 s[2:3], exec
	s_nop 0
	v_writelane_b32 v239, s6, 16
	s_nop 1
	v_writelane_b32 v239, s7, 17
	s_and_b64 s[6:7], s[2:3], s[6:7]
	s_mov_b64 exec, s[6:7]
	s_cbranch_execz .LBB0_5
	s_mov_b64 s[6:7], exec
	v_mbcnt_lo_u32_b32 v1, s6, 0
	v_mbcnt_hi_u32_b32 v1, s7, v1
	v_cmp_eq_u32_e32 vcc, 0, v1
	s_and_b64 s[8:9], exec, vcc
	s_mov_b64 exec, s[8:9]
	s_cbranch_execz .LBB0_5
	s_lshl_b32 s8, s78, 8
	s_bcnt1_i32_b64 s6, s[6:7]
	v_mov_b32_e32 v1, s8
	v_mov_b32_e32 v2, s6
	global_atomic_add v1, v2, s[58:59] offset:1024

.LBB0_400:
	s_cmp_lt_i32 s76, 2
	s_cselect_b64 s[6:7], -1, 0
	s_add_u32 s82, s58, 0x32100000
	s_addc_u32 s83, s59, 0
	s_and_b64 s[0:1], s[6:7], s[0:1]
	s_andn2_b64 vcc, exec, s[0:1]
	s_cbranch_vccnz .LBB0_417
	s_mov_b32 s101, s2
	s_cmpk_lt_i32 s96, 192
	s_cbranch_scc1 .Lh0_gemm
	s_sub_i32 s96, s96, 192
	s_movk_i32 s2, 64
	s_mov_b32 s98, 2
	s_mov_b32 s100, 5
	s_mov_b32 s99, 1
	s_branch .Lconv_entry

.LBB0_1568:
	s_and_b64 vcc, exec, s[0:1]
	s_cbranch_vccz .LBB0_1579
	s_cmpk_lt_i32 s96, 0x50
	s_cbranch_scc1 .LBB0_1579
	s_lshl_b32 s0, s96, 3
	s_addk_i32 s0, 0xfd80
	v_or_b32_e32 v1, s0, v186
	s_movk_i32 s0, 0x4200
	s_waitcnt vmcnt(0)
	v_and_b32_e32 v3, 7, v0
	v_mad_u32_u24 v6, v186, s0, 0
	s_movk_i32 s0, 0xe00
	v_bfe_u32 v18, v0, 3, 3
	v_lshlrev_b32_e32 v2, 4, v3
	v_mul_u32_u24_e32 v9, 0x840, v3
	v_mov_b32_e32 v3, 0
	s_lshl_b32 s3, s2, 3
	v_cmp_gt_i32_e64 s[4:5], s0, v1
	v_add_u32_e32 v7, v6, v2
	v_mul_u32_u24_e32 v8, 0x84, v18
	v_lshl_add_u64 v[4:5], s[58:59], 0, v[2:3]
	s_mov_b64 s[0:1], 0x100000
	s_mov_b32 s21, 0xe0000
	s_addk_i32 s3, 0xfd80
	v_lshl_add_u64 v[26:27], v[4:5], 0, s[0:1]
	v_lshlrev_b32_e32 v10, 2, v18
	s_mov_b64 s[0:1], 0x1c100000
	v_lshl_add_u64 v[30:31], s[90:91], 0, v[2:3]
	v_lshl_add_u64 v[32:33], s[92:93], 0, v[2:3]
	v_lshl_add_u64 v[34:35], s[94:95], 0, v[2:3]
	v_mul_u32_u24_e32 v2, 0x1c00, v18
	v_mul_lo_u32 v3, v1, s21
	v_add_u32_e32 v25, v7, v8
	s_mov_b32 s7, 0
	v_or_b32_e32 v20, 8, v18
	v_or_b32_e32 v22, 16, v18
	v_or_b32_e32 v24, 24, v18
	v_add3_u32 v19, v6, v9, v10
	v_lshl_add_u64 v[28:29], v[4:5], 0, s[0:1]
	s_movk_i32 s20, 0x1c00
	s_mov_b64 s[14:15], 5
	s_mov_b32 s98, 5
	s_mov_b64 s[10:11], 0
	v_or_b32_e32 v21, v2, v3
	s_mul_i32 s22, s3, 0xe0000
	v_lshlrev_b32_e32 v23, 7, v1
	s_lshl_b32 s23, s3, 7
	s_movk_i32 s24, 0x60
	s_mov_b32 s25, 0xff200000
	s_mov_b32 s26, 0x38000
	s_mov_b32 s27, 0x70000
	s_mov_b32 s28, 0xa8000
	s_mov_b32 s29, 0x118000
	s_mov_b32 s30, 0x150000
	s_mov_b32 s31, 0x188000
	s_mov_b32 s33, 0x1c0000
	s_mov_b32 s34, 0x1f8000
	s_mov_b32 s35, 0x230000
	s_mov_b32 s36, 0x268000
	s_mov_b32 s37, 0x2a0000
	s_mov_b32 s38, 0x2d8000
	s_mov_b32 s39, 0x310000
	s_mov_b32 s40, 0x348000
	v_add_u32_e32 v39, 0x420, v25
	v_add_u32_e32 v48, 0x428, v25
	v_add_u32_e32 v49, 0x840, v25
	v_add_u32_e32 v50, 0x848, v25
	v_add_u32_e32 v51, 0xc60, v25
	v_add_u32_e32 v52, 0xc68, v25
	v_add_u32_e32 v53, 0x1080, v25
	v_add_u32_e32 v54, 0x1088, v25
	v_add_u32_e32 v55, 0x14a0, v25
	v_add_u32_e32 v56, 0x14a8, v25
	v_add_u32_e32 v57, 0x18c0, v25
	v_add_u32_e32 v58, 0x18c8, v25
	v_add_u32_e32 v59, 0x1ce0, v25
	v_add_u32_e32 v60, 0x1ce8, v25
	v_add_u32_e32 v61, 0x2100, v25
	v_add_u32_e32 v62, 0x2108, v25
	v_add_u32_e32 v63, 0x2520, v25
	v_add_u32_e32 v64, 0x2528, v25
	v_add_u32_e32 v65, 0x2940, v25
	v_add_u32_e32 v66, 0x2948, v25
	v_add_u32_e32 v67, 0x2d60, v25
	v_add_u32_e32 v68, 0x2d68, v25
	s_mov_b32 s41, 0xc3e00000
	s_movk_i32 s42, 0xdff
	s_mov_b32 s43, 0x92492493
	s_movk_i32 s44, 0xe400
	v_add_u32_e32 v69, 0x3180, v25
	v_add_u32_e32 v70, 0x3188, v25
	v_add_u32_e32 v71, 0x35a0, v25
	v_add_u32_e32 v72, 0x35a8, v25
	v_add_u32_e32 v73, 0x39c0, v25
	v_add_u32_e32 v74, 0x39c8, v25
	v_mov_b32_e32 v75, 0x43e00000
	s_branch .LBB0_1572
.LBB0_1571:
	s_or_b64 exec, exec, s[12:13]
	s_add_u32 s98, s98, 1
	s_mov_b32 s14, s98
	s_mov_b32 s15, 0
	s_cmp_lt_u32 s98, 8
	s_cbranch_scc0 .LBB0_1579
